# bundle9 + up GEMM: next-unit gather index loads no longer waited (vmcnt(0)) at unit top; converted in last K iteration
# baseline (speedup 1.0000x reference)
.LBB0_826:
	v_cndmask_b32_e64 v0, 0, 1, s[22:23]
	v_cmp_ne_u32_e64 s[4:5], 1, v0
	s_andn2_b64 vcc, exec, s[22:23]
	s_mov_b32 s98, 0
	s_cbranch_vccnz .LBB0_828
	s_and_b32 s11, s12, -4
	s_add_i32 s11, s11, 0
	s_add_i32 s11, s11, 0x25000
	v_mov_b32_e32 v0, s11
	ds_read_b32 v0, v0
	s_ashr_i32 s11, s12, 2
	s_mul_hi_i32 s13, s11, 0x10100
	s_mul_i32 s11, s11, 0x10100
	v_mov_b32_e32 v2, s13
	s_waitcnt lgkmcnt(0)
	v_ashrrev_i32_e32 v1, 31, v0
	v_lshlrev_b64 v[0:1], 8, v[0:1]
	v_sub_co_u32_e32 v0, vcc, s11, v0
	v_readlane_b32 s14, v254, 46
	s_nop 0
	v_subb_co_u32_e32 v1, vcc, v2, v1, vcc
	s_ashr_i32 s11, s10, 31
	v_lshlrev_b64 v[0:1], 2, v[0:1]
	v_readlane_b32 s15, v254, 47
	s_nop 1
	v_lshl_add_u64 v[0:1], s[14:15], 0, v[0:1]
	s_lshl_b64 s[14:15], s[10:11], 10
	v_lshl_add_u64 v[0:1], v[0:1], 0, s[14:15]
	v_lshl_add_u64 v[2:3], v[194:195], 2, v[0:1]
	v_lshl_add_u64 v[0:1], v[196:197], 2, v[0:1]
	global_load_dword v220, v[2:3], off
	global_load_dword v221, v[0:1], off
	global_load_dword v222, v[0:1], off offset:512
	global_load_dword v223, v[2:3], off offset:512
	s_mov_b32 s98, 1

.LBB0_830:
	v_add_u32_e32 v0, 0, v208
	v_add_u32_e32 v1, 0x10000, v0
	v_add_u32_e32 v12, 0x14000, v0
	ds_read_b128 v[16:19], v1
	ds_read_b128 v[20:23], v1 offset:1024
	ds_read_b128 v[24:27], v1 offset:2048
	ds_read_b128 v[28:31], v1 offset:3072
	ds_read_b128 v[0:3], v12
	ds_read_b128 v[4:7], v12 offset:1024
	ds_read_b128 v[8:11], v12 offset:2048
	ds_read_b128 v[12:15], v12 offset:3072
	s_cmp_eq_u32 s51, 4
	s_cselect_b64 s[24:25], -1, 0
	s_add_i32 m0, s19, 0xc000
	s_add_u32 s22, s52, s20
	s_addc_u32 s23, s53, s21
	s_add_i32 s56, s19, 0xe000
	s_cmp_lg_u32 s51, 4
	v_mov_b32_e32 v64, v204
	ds_read_b128 v[56:59], v209
	ds_read_b128 v[60:63], v209 offset:1024
	ds_read_b128 v[48:51], v209 offset:2048
	ds_read_b128 v[52:55], v209 offset:3072
	ds_read_b128 v[40:43], v209 offset:4096
	ds_read_b128 v[44:47], v209 offset:5120
	ds_read_b128 v[32:35], v209 offset:6144
	ds_read_b128 v[36:39], v209 offset:7168
	s_nop 0
	global_load_lds_dwordx4 v64, s[22:23]
	v_mov_b32_e32 v64, v205
	s_mov_b32 m0, s56
	s_nop 0
	global_load_lds_dwordx4 v64, s[22:23]
	s_cbranch_scc1 .LBB0_829
	s_cmp_eq_u32 s98, 0
	s_cbranch_scc1 .Lupidx_skip
	s_waitcnt vmcnt(8)
	v_min_u32_e32 v220, 0xffff, v220
	v_min_u32_e32 v221, 0xffff, v221
	v_min_u32_e32 v222, 0xffff, v222
	v_min_u32_e32 v223, 0xffff, v223
	v_lshl_add_u32 v202, v220, 10, v198
	v_lshl_add_u32 v203, v221, 10, v200
	v_lshl_add_u32 v204, v223, 10, v198
	v_lshl_add_u32 v205, v222, 10, v200
.Lupidx_skip:
	s_branch .LBB0_829
.LBB0_832:
	s_and_b64 vcc, exec, s[8:9]
	s_cbranch_vccz .LBB0_834
	s_barrier
